# stack5: stack3 + routing wave issues both class-base atomics together and waits behind the combine-weight arithmetic
# speedup vs baseline: 1.0057x; 1.0057x over previous
; DEVINL void phase4(const Params& P, unsigned char* smem) {
;     ...
;             const float gwt = 1.f / (expf(g0 - gm) + expf(g1 - gm) + expf(g2 - gm) + expf(g3 - gm));
;             int i1 = 0, i2 = 0; float v1 = -3.0e38f, v2 = -3.0e38f;
;             for (int e = 0; e < 8; ++e) {
;                 const float v = LG(4 + gtop * 8 + e);
;                 if (v > v1) { v2 = v1; i2 = i1; v1 = v; i1 = e; } else if (v > v2) { v2 = v; i2 = e; }
;             }
;     ...
;             const float ex = expf(v2 - v1), w1 = gwt / (1.f + ex), w2 = gwt * ex / (1.f + ex);
;             const int ilo = i1 < i2 ? i1 : i2, ihi = i1 < i2 ? i2 : i1; const float wlo = i1 < i2 ? w1 : w2, whi = i1 < i2 ? w2 : w1;
;             const int cls = gtop * 28 + ilo * (15 - ilo) / 2 + (ihi - ilo - 1);
;             unsigned* s_cnt = (unsigned*)(smem + LDS_MISC);
;             s_cnt[t] = 0u; if (t < 48) s_cnt[64 + t] = 0u;
;             asm volatile("s_waitcnt lgkmcnt(0)" ::: "memory");
;             const unsigned lrk = atomicAdd(&s_cnt[cls], 1u);
;             asm volatile("s_waitcnt lgkmcnt(0)" ::: "memory");
;             { int tq = threadIdx.x; asm volatile("" : "+v"(tq));
;               const unsigned c0_ = s_cnt[tq]; s_cnt[128 + tq] = c0_ ? atomicAdd(&ccnt[tq * 64], c0_) : 0u;
;               if (tq < 48) { const unsigned c1_ = s_cnt[64 + tq]; s_cnt[192 + tq] = c1_ ? atomicAdd(&ccnt[(64 + tq) * 64], c1_) : 0u; } }
;             asm volatile("s_waitcnt vmcnt(0) lgkmcnt(0)" ::: "memory");
;             const unsigned pos = s_cnt[128 + cls] + lrk;
;             ctok[cls * NT + pos] = row; cw[cls * NT + pos] = (f32x2){wlo, whi};
.LBB0_579:
	s_or_b64 exec, exec, s[10:11]
	v_cndmask_b32_e32 v6, v6, v4, vcc
	v_sub_f32_e32 v3, v3, v6
	v_mul_f32_e32 v14, 0x3fb8aa3b, v3
	v_fma_f32 v15, v3, s76, -v14
	v_rndne_f32_e32 v16, v14
	v_fmac_f32_e32 v15, 0x32a5705f, v3
	v_sub_f32_e32 v14, v14, v16
	v_add_f32_e32 v14, v14, v15
	v_cvt_i32_f32_e32 v15, v16
	v_exp_f32_e32 v14, v14
	v_sub_f32_e32 v2, v2, v6
	v_cmp_ngt_f32_e32 vcc, s77, v3
	v_sub_f32_e32 v5, v5, v6
	v_ldexp_f32 v14, v14, v15
	v_mul_f32_e32 v15, 0x3fb8aa3b, v2
	v_fma_f32 v16, v2, s76, -v15
	v_rndne_f32_e32 v17, v15
	v_fmac_f32_e32 v16, 0x32a5705f, v2
	v_sub_f32_e32 v15, v15, v17
	v_add_f32_e32 v15, v15, v16
	v_exp_f32_e32 v15, v15
	v_cvt_i32_f32_e32 v16, v17
	v_cndmask_b32_e32 v14, 0, v14, vcc
	v_cmp_nlt_f32_e32 vcc, s78, v3
	v_sub_f32_e32 v4, v4, v6
	v_mul_f32_e32 v6, 0x3fb8aa3b, v4
	v_cndmask_b32_e32 v3, v224, v14, vcc
	v_ldexp_f32 v14, v15, v16
	v_mul_f32_e32 v15, 0x3fb8aa3b, v5
	v_fma_f32 v16, v5, s76, -v15
	v_rndne_f32_e32 v17, v15
	v_fmac_f32_e32 v16, 0x32a5705f, v5
	v_sub_f32_e32 v15, v15, v17
	v_add_f32_e32 v15, v15, v16
	v_exp_f32_e32 v15, v15
	v_cvt_i32_f32_e32 v16, v17
	v_cmp_ngt_f32_e32 vcc, s77, v2
	s_waitcnt vmcnt(0) lgkmcnt(0)
	s_nop 1
	v_cndmask_b32_e32 v14, 0, v14, vcc
	v_cmp_nlt_f32_e32 vcc, s78, v2
	s_nop 1
	v_cndmask_b32_e32 v2, v224, v14, vcc
	v_add_f32_e32 v2, v3, v2
	v_ldexp_f32 v3, v15, v16
	v_fma_f32 v14, v4, s76, -v6
	v_rndne_f32_e32 v15, v6
	v_fmac_f32_e32 v14, 0x32a5705f, v4
	v_sub_f32_e32 v6, v6, v15
	v_add_f32_e32 v6, v6, v14
	v_exp_f32_e32 v6, v6
	v_cvt_i32_f32_e32 v14, v15
	v_cmp_ngt_f32_e32 vcc, s77, v5
	s_nop 1
	v_cndmask_b32_e32 v3, 0, v3, vcc
	v_cmp_nlt_f32_e32 vcc, s78, v5
	s_nop 1
	v_cndmask_b32_e32 v3, v224, v3, vcc
	v_add_f32_e32 v2, v3, v2
	v_ldexp_f32 v3, v6, v14
	v_cmp_ngt_f32_e32 vcc, s77, v4
	s_nop 1
	v_cndmask_b32_e32 v3, 0, v3, vcc
	v_cmp_nlt_f32_e32 vcc, s78, v4
	s_nop 1
	v_cndmask_b32_e32 v3, v224, v3, vcc
	v_add_f32_e32 v2, v3, v2
	v_div_scale_f32 v3, s[8:9], v2, v2, 1.0
	v_rcp_f32_e32 v4, v3
	s_nop 0
	v_fma_f32 v5, -v3, v4, 1.0
	v_fmac_f32_e32 v4, v5, v4
	v_div_scale_f32 v5, vcc, 1.0, v2, 1.0
	v_mul_f32_e32 v6, v5, v4
	v_fma_f32 v14, -v3, v6, v5
	v_fmac_f32_e32 v6, v14, v4
	v_fma_f32 v3, -v3, v6, v5
	v_sub_f32_e32 v5, v11, v13
	v_mul_f32_e32 v11, 0x3fb8aa3b, v5
	v_fma_f32 v13, v5, s76, -v11
	v_rndne_f32_e32 v14, v11
	v_fmac_f32_e32 v13, 0x32a5705f, v5
	v_sub_f32_e32 v11, v11, v14
	v_add_f32_e32 v11, v11, v13
	v_exp_f32_e32 v11, v11
	v_cvt_i32_f32_e32 v13, v14
	v_div_fmas_f32 v3, v3, v4, v6
	v_div_fixup_f32 v2, v3, v2, 1.0
	v_cmp_ngt_f32_e32 vcc, s77, v5
	v_ldexp_f32 v3, v11, v13
	v_or_b32_e32 v11, s81, v0
	v_cndmask_b32_e32 v3, 0, v3, vcc
	v_cmp_nlt_f32_e32 vcc, s78, v5
	s_nop 1
	v_cndmask_b32_e32 v3, v224, v3, vcc
	v_add_f32_e32 v4, 1.0, v3
	v_div_scale_f32 v5, s[8:9], v4, v4, v2
	v_rcp_f32_e32 v6, v5
	v_mul_f32_e32 v3, v2, v3
	v_fma_f32 v13, -v5, v6, 1.0
	v_fmac_f32_e32 v6, v13, v6
	v_div_scale_f32 v13, vcc, v2, v4, v2
	v_mul_f32_e32 v14, v13, v6
	v_fma_f32 v15, -v5, v14, v13
	v_fmac_f32_e32 v14, v15, v6
	v_fma_f32 v5, -v5, v14, v13
	v_div_scale_f32 v13, s[8:9], v4, v4, v3
	v_rcp_f32_e32 v15, v13
	v_div_fmas_f32 v5, v5, v6, v14
	v_div_fixup_f32 v5, v5, v4, v2
	v_fma_f32 v2, -v13, v15, 1.0
	v_fmac_f32_e32 v15, v2, v15
	v_div_scale_f32 v2, vcc, v3, v4, v3
	v_mul_f32_e32 v6, v2, v15
	v_fma_f32 v14, -v13, v6, v2
	v_fmac_f32_e32 v6, v14, v15
	v_fma_f32 v2, -v13, v6, v2
	v_div_fmas_f32 v2, v2, v15, v6
	v_div_fixup_f32 v3, v2, v4, v3
	s_waitcnt vmcnt(0)
	ds_write_b32 v36, v32 offset:512
	s_and_saveexec_b64 s[14:15], s[12:13]
	ds_write_b32 v36, v33 offset:768
	s_or_b64 exec, exec, s[14:15]
	ds_read_b32 v4, v12 offset:512
	v_cmp_lt_u32_e32 vcc, v8, v10
	s_nop 1
	v_cndmask_b32_e32 v2, v3, v5, vcc
	v_cndmask_b32_e32 v3, v5, v3, vcc
	v_lshlrev_b32_e32 v5, 14, v7
	s_waitcnt lgkmcnt(0)
	v_add3_u32 v178, v9, v5, v4
	v_lshl_add_u64 v[4:5], v[178:179], 2, s[20:21]
	global_store_dword v[4:5], v11, off
	v_lshl_add_u64 v[4:5], v[178:179], 3, s[22:23]
	global_store_dwordx2 v[4:5], v[2:3], off

; DEVINL void phase4(const Params& P, unsigned char* smem) {
;     ...
;             const int cls = gtop * 28 + ilo * (15 - ilo) / 2 + (ihi - ilo - 1);
;             unsigned* s_cnt = (unsigned*)(smem + LDS_MISC);
;             s_cnt[t] = 0u; if (t < 48) s_cnt[64 + t] = 0u;
;             asm volatile("s_waitcnt lgkmcnt(0)" ::: "memory");
;             const unsigned lrk = atomicAdd(&s_cnt[cls], 1u);
;             asm volatile("s_waitcnt lgkmcnt(0)" ::: "memory");
;             { int tq = threadIdx.x; asm volatile("" : "+v"(tq));
;               const unsigned c0_ = s_cnt[tq]; s_cnt[128 + tq] = c0_ ? atomicAdd(&ccnt[tq * 64], c0_) : 0u;
;               if (tq < 48) { const unsigned c1_ = s_cnt[64 + tq]; s_cnt[192 + tq] = c1_ ? atomicAdd(&ccnt[(64 + tq) * 64], c1_) : 0u; } }
;             asm volatile("s_waitcnt vmcnt(0) lgkmcnt(0)" ::: "memory");
.LBB0_633:
	s_or_b64 exec, exec, s[10:11]
	ds_write_b32 v225, v179
	s_and_saveexec_b64 s[8:9], s[6:7]
	v_add_u32_e32 v9, 0x100, v225
	ds_write_b32 v9, v179
	s_or_b64 exec, exec, s[8:9]
	v_min_u32_e32 v9, v8, v10
	v_xor_b32_e32 v14, 15, v9
	v_mul_u32_u24_e32 v14, v14, v9
	v_not_b32_e32 v9, v9
	v_max_u32_e32 v12, v8, v10
	v_lshrrev_b32_e32 v14, 1, v14
	v_mad_u32_u24 v7, v7, 28, v9
	v_add3_u32 v7, v7, v12, v14
	s_waitcnt lgkmcnt(0)
	v_lshl_add_u32 v12, v7, 2, s57
	v_mov_b32_e32 v9, 1
	ds_add_rtn_u32 v9, v12, v9
	v_mov_b32_e32 v15, v0
	s_waitcnt lgkmcnt(0)
	v_lshl_add_u32 v36, v15, 2, s57
	ds_read_b32 v30, v36
	ds_read_b32 v31, v36 offset:256
	v_mov_b32_e32 v32, 0
	v_mov_b32_e32 v33, 0
	v_cmp_gt_i32_e64 s[12:13], 48, v15
	s_mov_b64 s[10:11], exec
	s_waitcnt lgkmcnt(0)
	v_cmp_ne_u32_e64 s[8:9], 0, v30
	v_cmp_ne_u32_e64 s[14:15], 0, v31
	s_nop 1
	s_and_b64 s[14:15], s[14:15], s[12:13]
	s_and_b64 exec, s[10:11], s[8:9]
	s_cbranch_execz .Lp4_r_noa0
	v_lshlrev_b32_e32 v34, 6, v15
	v_ashrrev_i32_e32 v35, 31, v34
	v_lshl_add_u64 v[34:35], v[34:35], 2, s[18:19]
	global_atomic_add v32, v[34:35], v30, off sc0
.Lp4_r_noa0:
	s_and_b64 exec, s[10:11], s[14:15]
	s_cbranch_execz .Lp4_r_noa1
	v_mov_b32_e32 v34, 0x1000
	v_lshl_add_u32 v34, v15, 6, v34
	v_ashrrev_i32_e32 v35, 31, v34
	v_lshl_add_u64 v[34:35], v[34:35], 2, s[18:19]
	global_atomic_add v33, v[34:35], v31, off sc0
.Lp4_r_noa1:
	s_mov_b64 exec, s[10:11]
	s_branch .LBB0_579
